# MLA fast88 loop: permanent all-ones fp8 operand in unused VGPRs (no per-tile rematerialisation), dead zero-inits removed, hoisted K reads, deferred PV MFMA
# speedup vs baseline: 1.0109x; 1.0065x over previous
; #define ALAS __attribute__((address_space(3)))
; #define ATT_WAIT_BAR() asm volatile("s_waitcnt vmcnt(0) lgkmcnt(0)\n\ts_barrier" ::: "memory")
; #define MF_ISSUE_K(t, s) do { glds16(ksrc + (long)(t) * 64 * 512, (unsigned)__builtin_amdgcn_readfirstlane(kdst + (s) * KSLOT)); \
;         if (wid < 4) glds16(krsrc + (long)(t) * 64 * 32, (unsigned)__builtin_amdgcn_readfirstlane(krdst + (s) * KSLOT)); } while (0)
; #define MF_ISSUE_V(t, s) glds16(vsrc + (long)(t) * 64 * 512, (unsigned)__builtin_amdgcn_readfirstlane(vdst + (s) * VSLOT))
; __device__ __forceinline__ bool mla_unit_fast88(const Args& A, int b, int h, int qb, ALAS char* shm, const int tidb) {
;     ...
;     MF_ISSUE_K(0, 0); MF_ISSUE_V(0, 0); MF_ISSUE_K(1, 1);
;     const unsigned char* Q8w = A.Q8 + (rowbase + q0 + wid * 32 + r32) * 768 + h * 96;
;     const unsigned char* Q8r = hi == 0 ? Q8w + 64 : A.ZERO;
;     v8i qf0, qf1;
;     { const u32x4 a0 = *(const u32x4*)(Q8w + 32 * hi), a1 = *(const u32x4*)(Q8w + 32 * hi + 16), b0 = *(const u32x4*)(Q8r), b1 = *(const u32x4*)(Q8r + 16);
;       qf0 = (v8i){(int)a0.x, (int)a0.y, (int)a0.z, (int)a0.w, (int)a1.x, (int)a1.y, (int)a1.z, (int)a1.w}; qf1 = (v8i){(int)b0.x, (int)b0.y, (int)b0.z, (int)b0.w, (int)b1.x, (int)b1.y, (int)b1.z, (int)b1.w}; }
;     const int sa8 = 0x7c7c7c7c, sb8 = 0x7b7b7b7b;
;     f32x16 o0 = {}, o1 = {}, ls = {};
;     const v8i ones8 = {0x38383838, 0x38383838, 0x38383838, 0x38383838, 0x38383838, 0x38383838, 0x38383838, 0x38383838};
;     const int vbo = ((lane >> 4) & 1) * 32 + (lane & 3) * 8 + (4 * hi + ((lane & 15) >> 2)) * 64;
;     ALAS const char* Kfr = shm + L_K + lane * 16;
;     ...
;     ATT_WAIT_BAR();
;     f32x16 cs[2][2];
;     { f32x16 z0 = {}, z1 = {}; ALAS const char* Ks_ = Kfr;
;       v8i k00, k01, k10, k11; M8_KFRAG(k00, Ks_, 0, 0); M8_KFRAG(k01, Ks_, 0, 1); M8_KFRAG(k10, Ks_, 1, 0); M8_KFRAG(k11, Ks_, 1, 1);
;       mfma8_acc(z0, k00, qf0, sa8, sb8); mfma8_acc(z1, k01, qf0, sa8, sb8); mfma8_acc(z0, k10, qf1, sa8, sb8); mfma8_acc(z1, k11, qf1, sa8, sb8);
;       asm volatile("s_nop 15\n\ts_nop 7" : "+v"(z0), "+v"(z1));
;       cs[0][0] = z0; cs[0][1] = z1; }
;     const float mhat = MF_ROWMAX(cs[0][0], cs[0][1]);
; #pragma unroll
;     for (int r = 0; r < 16; ++r) { cs[0][0][r] -= mhat; cs[0][1][r] -= mhat; }
;     f32x16 negm;
; #pragma unroll
;     for (int r = 0; r < 16; ++r) negm[r] = -mhat;
.LBB0_648:
	v_cmp_gt_u32_e32 vcc, 32, v154
	v_mov_b32_e32 v2, 0x800
	v_mov_b32_e32 v3, 0x8000
	v_cndmask_b32_e32 v2, 0, v2, vcc
	v_cndmask_b32_e64 v100, v2, v3, s[2:3]
	s_lshl_b32 s2, s6, 8
	v_mov_b32_e32 v101, v1
	s_lshl_b32 s37, s6, 2
	s_add_i32 s3, s45, 0x2000
	s_or_b32 s36, s30, s2
	s_lshl_b32 s2, s1, 5
	s_add_i32 s0, s37, 4
	s_add_i32 s47, s47, s37
	v_lshl_add_u64 v[2:3], v[146:147], 0, v[100:101]
	s_mov_b32 s4, m0
	s_mov_b32 m0, s3
	s_nop 0
	global_load_lds_dwordx4 v[2:3], off
	s_mov_b32 m0, s4
	s_ashr_i32 s3, s2, 31
	s_add_u32 s24, s36, s2
	v_or_b32_e32 v4, s24, v156
	v_mov_b64_e32 v[2:3], s[74:75]
	s_addc_u32 s25, s31, s3
	v_mad_u64_u32 v[2:3], s[2:3], v4, s67, v[2:3]
	v_mov_b32_e32 v4, 0x300
	v_mad_i32_i24 v3, s25, v4, v3
	v_lshl_add_u64 v[4:5], v[2:3], 0, 64
	v_mov_b32_e32 v6, s27
	v_cndmask_b32_e32 v5, v6, v5, vcc
	v_mov_b32_e32 v6, s26
	v_lshl_add_u64 v[2:3], v[2:3], 0, v[0:1]
	v_cndmask_b32_e32 v4, v6, v4, vcc
	global_load_dwordx4 v[134:137], v[2:3], off offset:16
	global_load_dwordx4 v[130:133], v[2:3], off
	global_load_dwordx4 v[142:145], v[4:5], off offset:16
	global_load_dwordx4 v[138:141], v[4:5], off
	v_lshlrev_b32_e32 v155, 4, v154
	s_mov_b32 s4, 0
	v_add_u32_e32 v157, 0, v155
	s_waitcnt vmcnt(0) lgkmcnt(0)
	s_barrier
	s_mov_b32 s18, s4
	s_mov_b32 s19, s4
	ds_read_b128 v[50:53], v157
	ds_read_b128 v[54:57], v157 offset:1024
	ds_read_b128 v[58:61], v157 offset:2048
	ds_read_b128 v[62:65], v157 offset:3072
	ds_read_b128 v[66:69], v157 offset:4096
	ds_read_b128 v[70:73], v157 offset:5120
	ds_read_b128 v[74:77], v157 offset:6144
	ds_read_b128 v[78:81], v157 offset:7168
	s_mov_b32 s5, s4
	s_mov_b32 s6, s4
	s_mov_b32 s7, s4
	s_mov_b32 s8, s4
	s_mov_b32 s9, s4
	s_mov_b32 s10, s4
	s_mov_b32 s11, s4
	s_mov_b32 s12, s4
	s_mov_b32 s13, s4
	s_mov_b32 s14, s4
	s_mov_b32 s15, s4
	s_mov_b32 s16, s4
	s_mov_b32 s17, s4
	v_mov_b64_e32 v[32:33], s[18:19]
	v_mov_b64_e32 v[30:31], s[16:17]
	v_mov_b64_e32 v[28:29], s[14:15]
	v_mov_b64_e32 v[26:27], s[12:13]
	v_mov_b64_e32 v[24:25], s[10:11]
	v_mov_b64_e32 v[22:23], s[8:9]
	v_mov_b64_e32 v[20:21], s[6:7]
	v_mov_b64_e32 v[18:19], s[4:5]
	v_mov_b64_e32 v[48:49], v[32:33]
	v_mov_b64_e32 v[46:47], v[30:31]
	v_mov_b64_e32 v[44:45], v[28:29]
	v_mov_b64_e32 v[42:43], v[26:27]
	v_mov_b64_e32 v[40:41], v[24:25]
	v_mov_b64_e32 v[38:39], v[22:23]
	v_mov_b64_e32 v[36:37], v[20:21]
	v_mov_b64_e32 v[34:35], v[18:19]
	v_mov_b32_e32 v16, v1
	v_mov_b32_e32 v17, v1
	v_mov_b32_e32 v2, v1
	v_mov_b32_e32 v3, v1
	v_mov_b32_e32 v4, v1
	v_mov_b32_e32 v5, v1
	v_mov_b32_e32 v6, v1
	v_mov_b32_e32 v7, v1
	v_mov_b32_e32 v8, v1
	v_mov_b32_e32 v9, v1
	v_mov_b32_e32 v10, v1
	v_mov_b32_e32 v11, v1
	v_mov_b32_e32 v12, v1
	v_mov_b32_e32 v13, v1
	v_mov_b32_e32 v14, v1
	v_mov_b32_e32 v15, v1
	s_mov_b32 s41, s31
	s_mov_b32 s5, 3
	v_mul_hi_u32_u24_e32 v149, 3, v100
	v_mul_u32_u24_e32 v148, 3, v100
	v_lshl_add_u64 v[150:151], v[98:99], 0, s[78:79]
	s_waitcnt vmcnt(0) lgkmcnt(0)
	v_mfma_scale_f32_32x32x64_f8f6f4 v[34:49], v[50:57], v[130:137], v[34:49], v247, v253 op_sel_hi:[0,0,0]
	s_waitcnt lgkmcnt(4)
	v_mfma_scale_f32_32x32x64_f8f6f4 v[18:33], v[58:65], v[130:137], v[18:33], v247, v253 op_sel_hi:[0,0,0]
	s_waitcnt vmcnt(0) lgkmcnt(2)
	v_mfma_scale_f32_32x32x64_f8f6f4 v[34:49], v[66:73], v[138:145], v[34:49], v247, v253 op_sel_hi:[0,0,0]
	s_waitcnt lgkmcnt(0)
	v_mfma_scale_f32_32x32x64_f8f6f4 v[18:33], v[74:81], v[138:145], v[18:33], v247, v253 op_sel_hi:[0,0,0]
	s_nop 0
	s_nop 15
	s_nop 7
	s_nop 0
	v_max3_f32 v0, v34, v18, v38
	s_nop 0
	v_max3_f32 v0, v0, v22, v42
	s_nop 0
	v_max3_f32 v0, v0, v26, v46
	s_nop 0
	v_max_f32_e32 v0, v0, v30
	v_max3_f32 v50, v35, v19, v39
	s_nop 0
	v_max3_f32 v50, v50, v23, v43
	s_nop 0
	v_max3_f32 v50, v50, v27, v47
	s_nop 0
	v_max_f32_e32 v50, v50, v31
	v_max3_f32 v51, v36, v20, v40
	s_nop 0
	v_max3_f32 v51, v51, v24, v44
	s_nop 0
	v_max3_f32 v51, v51, v28, v48
	s_nop 0
	v_max_f32_e32 v51, v51, v32
	v_max3_f32 v52, v37, v21, v41
	s_nop 0
	v_max3_f32 v52, v52, v25, v45
	s_nop 0
	v_max3_f32 v52, v52, v29, v49
	s_nop 0
	v_max_f32_e32 v52, v52, v33
	v_max3_f32 v0, v0, v50, v51
	s_nop 0
	v_max_f32_e32 v0, v0, v52
	s_nop 0
	v_mov_b32_e32 v50, v0
	s_nop 1
	v_permlane32_swap_b32_e32 v0, v50
	v_max_f32_e32 v50, v50, v50
	v_max_f32_e32 v0, v0, v0
	v_max_f32_e32 v0, v0, v50
	v_sub_f32_e32 v65, v49, v0
	v_sub_f32_e32 v64, v48, v0
	v_sub_f32_e32 v63, v47, v0
	v_sub_f32_e32 v62, v46, v0
	v_sub_f32_e32 v61, v45, v0
	v_sub_f32_e32 v60, v44, v0
	v_sub_f32_e32 v59, v43, v0
	v_sub_f32_e32 v58, v42, v0
	v_sub_f32_e32 v57, v41, v0
	v_sub_f32_e32 v56, v40, v0
	v_sub_f32_e32 v55, v39, v0
	v_sub_f32_e32 v54, v38, v0
	v_sub_f32_e32 v53, v37, v0
	v_sub_f32_e32 v52, v36, v0
	v_sub_f32_e32 v51, v35, v0
	v_sub_f32_e32 v50, v34, v0
	v_sub_f32_e32 v97, v33, v0
	v_sub_f32_e32 v96, v32, v0
	v_sub_f32_e32 v95, v31, v0
	v_sub_f32_e32 v94, v30, v0
	v_sub_f32_e32 v93, v29, v0
	v_sub_f32_e32 v92, v28, v0
	v_sub_f32_e32 v91, v27, v0
	v_sub_f32_e32 v90, v26, v0
	v_sub_f32_e32 v89, v25, v0
	v_sub_f32_e32 v88, v24, v0
	v_sub_f32_e32 v87, v23, v0
	v_sub_f32_e32 v86, v22, v0
	v_sub_f32_e32 v85, v21, v0
	v_sub_f32_e32 v84, v20, v0
	v_sub_f32_e32 v83, v19, v0
	v_sub_f32_e32 v82, v18, v0
	v_xor_b32_e32 v66, 0x80000000, v0
	v_mov_b64_e32 v[32:33], v[16:17]
	v_mov_b64_e32 v[48:49], v[16:17]
	v_mov_b32_e32 v67, v66
	v_mov_b32_e32 v68, v66
	v_mov_b32_e32 v69, v66
	v_mov_b32_e32 v70, v66
	v_mov_b32_e32 v71, v66
	v_mov_b32_e32 v72, v66
	v_mov_b32_e32 v73, v66
	v_mov_b32_e32 v74, v66
	v_mov_b32_e32 v75, v66
	v_mov_b32_e32 v76, v66
	v_mov_b32_e32 v77, v66
	v_mov_b32_e32 v78, v66
	v_mov_b32_e32 v79, v66
	v_mov_b32_e32 v80, v66
	v_mov_b32_e32 v81, v66
	v_lshlrev_b32_e32 v0, 1, v100
	v_mov_b64_e32 v[30:31], v[14:15]
	v_mov_b64_e32 v[28:29], v[12:13]
	v_mov_b64_e32 v[26:27], v[10:11]
	v_mov_b64_e32 v[24:25], v[8:9]
	v_mov_b64_e32 v[22:23], v[6:7]
	v_mov_b64_e32 v[20:21], v[4:5]
	v_mov_b64_e32 v[18:19], v[2:3]
	v_mov_b64_e32 v[46:47], v[14:15]
	v_mov_b64_e32 v[44:45], v[12:13]
	v_mov_b64_e32 v[42:43], v[10:11]
	v_mov_b64_e32 v[40:41], v[8:9]
	v_mov_b64_e32 v[38:39], v[6:7]
	v_mov_b64_e32 v[36:37], v[4:5]
	v_mov_b64_e32 v[34:35], v[2:3]
	v_mov_b32_e32 v172, 0
	v_mov_b32_e32 v173, 0
	v_mov_b32_e32 v174, 0
	v_mov_b32_e32 v175, 0
	v_mov_b32_e32 v176, 0
	v_mov_b32_e32 v177, 0
	v_mov_b32_e32 v178, 0
	v_mov_b32_e32 v179, 0
	v_mov_b32_e32 v180, 0
	v_mov_b32_e32 v181, 0
	v_mov_b32_e32 v182, 0
	v_mov_b32_e32 v183, 0
	v_mov_b32_e32 v184, 0
	v_mov_b32_e32 v185, 0
	v_mov_b32_e32 v186, 0
	v_mov_b32_e32 v187, 0
	v_mov_b32_e32 v196, v162
	v_mov_b32_e32 v197, v162
	v_mov_b32_e32 v198, v162
	v_mov_b32_e32 v199, v162
	v_mov_b32_e32 v200, v162
	v_mov_b32_e32 v201, v162
	v_mov_b32_e32 v202, v162
	v_mov_b32_e32 v203, v162

; __device__ __forceinline__ bool mla_unit_fast88(const Args& A, int b, int h, int qb, ALAS char* shm, const int tidb) {
;     ...
;             if (t + 2 < t_end) MF_ISSUE_K(t + 2, ks2);
;             if (t + 1 < t_end) MF_ISSUE_V(t + 1, vs ^ 1);
;             if (vis) {
;                 {
;                     ALAS const char* Ks_ = Kfr + ks1 * KSLOT;
;                     v8i kfa, kfb; M8_KFRAG(kfa, Ks_, 0, 0);
;                     M8_KFRAG(kfb, Ks_, 0, 1);
;                     mfma8_new(N0, kfa, qf0, negm, sa8, sb8);
; #pragma unroll
;                     for (int e = 0; e < 8; ++e) C0[e] = __builtin_amdgcn_exp2f(C0[e]);
;                     __builtin_amdgcn_sched_barrier(0);
;                     M8_KFRAG(kfa, Ks_, 1, 0);
;                     mfma8_new(N1, kfb, qf0, negm, sa8, sb8);
; #pragma unroll
;                     for (int e = 8; e < 16; ++e) C0[e] = __builtin_amdgcn_exp2f(C0[e]);
;                     __builtin_amdgcn_sched_barrier(0);
;                     M8_KFRAG(kfb, Ks_, 1, 1);
;                     mfma8_acc(N0, kfa, qf1, sa8, sb8);
; #pragma unroll
;                     for (int e = 0; e < 8; ++e) C1[e] = __builtin_amdgcn_exp2f(C1[e]);
;                     __builtin_amdgcn_sched_barrier(0);
;                     mfma8_acc(N1, kfb, qf1, sa8, sb8);
; #pragma unroll
;                     for (int e = 8; e < 16; ++e) C1[e] = __builtin_amdgcn_exp2f(C1[e]);
;                     __builtin_amdgcn_sched_barrier(0);
;                 }
;                 ALAS const char* vb_ = shm + L_V + vs * 4096 + lane * 16;
;                 v8i vf0, vf1;
;                 { const u32x4 a0 = *(ALAS const u32x4*)(vb_), a1 = *(ALAS const u32x4*)(vb_ + 1024), b0 = *(ALAS const u32x4*)(vb_ + 2048), b1 = *(ALAS const u32x4*)(vb_ + 3072);
;                   vf0 = (v8i){(int)a0.x, (int)a0.y, (int)a0.z, (int)a0.w, (int)a1.x, (int)a1.y, (int)a1.z, (int)a1.w}; vf1 = (v8i){(int)b0.x, (int)b0.y, (int)b0.z, (int)b0.w, (int)b1.x, (int)b1.y, (int)b1.z, (int)b1.w}; }
;                 v8i pf;
; #pragma unroll
;                 for (int kk = 0; kk < 4; ++kk) { const f32x16& cc_ = (kk < 2) ? C0 : C1; const int k8_ = 8 * (kk & 1);
;                     int w0_ = 0, w1_ = 0;
;                     w0_ = __builtin_amdgcn_cvt_pk_bf8_f32(cc_[k8_], cc_[k8_ + 1], w0_, false); w0_ = __builtin_amdgcn_cvt_pk_bf8_f32(cc_[k8_ + 2], cc_[k8_ + 3], w0_, true);
.LBB0_653:
	s_add_i32 s7, s5, -3
	s_cmp_gt_i32 s7, s47
	s_cbranch_scc1 .Lmla_nv0
	v_lshl_add_u32 v158, s4, 13, v157
	v_exp_f32_e32 v50, v50
	v_exp_f32_e32 v51, v51
	v_exp_f32_e32 v52, v52
	v_exp_f32_e32 v53, v53
	v_exp_f32_e32 v54, v54
	v_exp_f32_e32 v55, v55
	v_exp_f32_e32 v56, v56
	v_exp_f32_e32 v57, v57
	s_waitcnt lgkmcnt(2)
	v_mfma_scale_f32_32x32x64_f8f6f4 v[98:113], v[114:121], v[130:137], v[66:81], v247, v253 op_sel_hi:[0,0,0]
	ds_read_b128 v[172:175], v158 offset:4096
	ds_read_b128 v[176:179], v158 offset:5120
	v_exp_f32_e32 v58, v58
	v_exp_f32_e32 v59, v59
	v_exp_f32_e32 v60, v60
	v_exp_f32_e32 v61, v61
	v_exp_f32_e32 v62, v62
	v_exp_f32_e32 v63, v63
	v_exp_f32_e32 v64, v64
	v_exp_f32_e32 v65, v65
	s_waitcnt lgkmcnt(2)
	v_mfma_scale_f32_32x32x64_f8f6f4 v[114:129], v[164:171], v[130:137], v[66:81], v247, v253 op_sel_hi:[0,0,0]
	ds_read_b128 v[164:167], v158 offset:6144
	ds_read_b128 v[168:171], v158 offset:7168
	v_exp_f32_e32 v82, v82
	v_exp_f32_e32 v83, v83
	v_exp_f32_e32 v84, v84
	v_exp_f32_e32 v85, v85
	v_exp_f32_e32 v86, v86
	v_exp_f32_e32 v87, v87
	v_exp_f32_e32 v88, v88
	v_exp_f32_e32 v89, v89
	s_waitcnt lgkmcnt(2)
	v_mfma_scale_f32_32x32x64_f8f6f4 v[98:113], v[172:179], v[138:145], v[98:113], v247, v253 op_sel_hi:[0,0,0]
	v_exp_f32_e32 v90, v90
	v_exp_f32_e32 v91, v91
	v_exp_f32_e32 v92, v92
	v_exp_f32_e32 v93, v93
	v_exp_f32_e32 v94, v94
	v_exp_f32_e32 v95, v95
	v_exp_f32_e32 v96, v96
	v_exp_f32_e32 v97, v97
	s_waitcnt lgkmcnt(0)
	v_mfma_scale_f32_32x32x64_f8f6f4 v[114:129], v[164:171], v[138:145], v[114:129], v247, v253 op_sel_hi:[0,0,0]
	ds_read_b128 v[164:167], v157 offset:36864
	ds_read_b128 v[168:171], v157 offset:37888
	ds_read_b128 v[172:175], v157 offset:38912
	ds_read_b128 v[176:179], v157 offset:39936
	v_cvt_pk_bf8_f32 v180, v50, v51
	v_cvt_pk_bf8_f32 v181, v54, v55
	v_cvt_pk_bf8_f32 v182, v58, v59
	v_cvt_pk_bf8_f32 v183, v62, v63
	v_cvt_pk_bf8_f32 v184, v82, v83
	v_cvt_pk_bf8_f32 v185, v86, v87
	v_cvt_pk_bf8_f32 v186, v90, v91
	v_cvt_pk_bf8_f32 v187, v94, v95
	v_cvt_pk_bf8_f32 v180, v52, v53 op_sel:[0,0,1]
	v_cvt_pk_bf8_f32 v181, v56, v57 op_sel:[0,0,1]
	v_cvt_pk_bf8_f32 v182, v60, v61 op_sel:[0,0,1]
	v_cvt_pk_bf8_f32 v183, v64, v65 op_sel:[0,0,1]
	v_cvt_pk_bf8_f32 v184, v84, v85 op_sel:[0,0,1]
	v_cvt_pk_bf8_f32 v185, v88, v89 op_sel:[0,0,1]
	v_cvt_pk_bf8_f32 v186, v92, v93 op_sel:[0,0,1]
	v_cvt_pk_bf8_f32 v187, v96, v97 op_sel:[0,0,1]
	s_waitcnt lgkmcnt(2)
	v_mfma_scale_f32_32x32x64_f8f6f4 v[2:17], v[180:187], v[164:171], v[2:17], v251, v247 op_sel_hi:[0,0,0] cbsz:1
	s_waitcnt lgkmcnt(0)
	v_mfma_scale_f32_32x32x64_f8f6f4 v[34:49], v[180:187], v[196:203], v[34:49], v251, v251 op_sel_hi:[0,0,0] cbsz:1

; __device__ __forceinline__ bool mla_unit_fast88(const Args& A, int b, int h, int qb, ALAS char* shm, const int tidb) {
;     ...
;             if (t + 2 < t_end) MF_ISSUE_K(t + 2, ks2);
;             if (t + 1 < t_end) MF_ISSUE_V(t + 1, vs ^ 1);
;             if (vis) {
;                 {
;                     ALAS const char* Ks_ = Kfr + ks1 * KSLOT;
;                     v8i kfa, kfb; M8_KFRAG(kfa, Ks_, 0, 0);
;                     M8_KFRAG(kfb, Ks_, 0, 1);
;                     mfma8_new(N0, kfa, qf0, negm, sa8, sb8);
; #pragma unroll
;                     for (int e = 0; e < 8; ++e) C0[e] = __builtin_amdgcn_exp2f(C0[e]);
;                     __builtin_amdgcn_sched_barrier(0);
;                     M8_KFRAG(kfa, Ks_, 1, 0);
;                     mfma8_new(N1, kfb, qf0, negm, sa8, sb8);
; #pragma unroll
;                     for (int e = 8; e < 16; ++e) C0[e] = __builtin_amdgcn_exp2f(C0[e]);
;                     __builtin_amdgcn_sched_barrier(0);
;                     M8_KFRAG(kfb, Ks_, 1, 1);
;                     mfma8_acc(N0, kfa, qf1, sa8, sb8);
; #pragma unroll
;                     for (int e = 0; e < 8; ++e) C1[e] = __builtin_amdgcn_exp2f(C1[e]);
;                     __builtin_amdgcn_sched_barrier(0);
;                     mfma8_acc(N1, kfb, qf1, sa8, sb8);
; #pragma unroll
;                     for (int e = 8; e < 16; ++e) C1[e] = __builtin_amdgcn_exp2f(C1[e]);
;                     __builtin_amdgcn_sched_barrier(0);
;                 }
;                 ALAS const char* vb_ = shm + L_V + vs * 4096 + lane * 16;
;                 v8i vf0, vf1;
;                 { const u32x4 a0 = *(ALAS const u32x4*)(vb_), a1 = *(ALAS const u32x4*)(vb_ + 1024), b0 = *(ALAS const u32x4*)(vb_ + 2048), b1 = *(ALAS const u32x4*)(vb_ + 3072);
;                   vf0 = (v8i){(int)a0.x, (int)a0.y, (int)a0.z, (int)a0.w, (int)a1.x, (int)a1.y, (int)a1.z, (int)a1.w}; vf1 = (v8i){(int)b0.x, (int)b0.y, (int)b0.z, (int)b0.w, (int)b1.x, (int)b1.y, (int)b1.z, (int)b1.w}; }
;                 v8i pf;
; #pragma unroll
;                 for (int kk = 0; kk < 4; ++kk) { const f32x16& cc_ = (kk < 2) ? C0 : C1; const int k8_ = 8 * (kk & 1);
;                     int w0_ = 0, w1_ = 0;
;                     w0_ = __builtin_amdgcn_cvt_pk_bf8_f32(cc_[k8_], cc_[k8_ + 1], w0_, false); w0_ = __builtin_amdgcn_cvt_pk_bf8_f32(cc_[k8_ + 2], cc_[k8_ + 3], w0_, true);
.LBB0_658:
	v_lshl_add_u32 v146, s4, 13, v157
	v_exp_f32_e32 v98, v98
	v_exp_f32_e32 v99, v99
	v_exp_f32_e32 v100, v100
	v_exp_f32_e32 v101, v101
	v_exp_f32_e32 v102, v102
	v_exp_f32_e32 v103, v103
	v_exp_f32_e32 v104, v104
	v_exp_f32_e32 v105, v105
	s_waitcnt lgkmcnt(2)
	v_mfma_scale_f32_32x32x64_f8f6f4 v[50:65], v[82:89], v[130:137], v[66:81], v247, v253 op_sel_hi:[0,0,0]
	ds_read_b128 v[172:175], v146 offset:4096
	ds_read_b128 v[176:179], v146 offset:5120
	v_exp_f32_e32 v106, v106
	v_exp_f32_e32 v107, v107
	v_exp_f32_e32 v108, v108
	v_exp_f32_e32 v109, v109
	v_exp_f32_e32 v110, v110
	v_exp_f32_e32 v111, v111
	v_exp_f32_e32 v112, v112
	v_exp_f32_e32 v113, v113
	s_waitcnt lgkmcnt(2)
	v_mfma_scale_f32_32x32x64_f8f6f4 v[82:97], v[164:171], v[130:137], v[66:81], v247, v253 op_sel_hi:[0,0,0]
	ds_read_b128 v[164:167], v146 offset:6144
	ds_read_b128 v[168:171], v146 offset:7168
	v_exp_f32_e32 v114, v114
	v_exp_f32_e32 v115, v115
	v_exp_f32_e32 v116, v116
	v_exp_f32_e32 v117, v117
	v_exp_f32_e32 v118, v118
	v_exp_f32_e32 v119, v119
	v_exp_f32_e32 v120, v120
	v_exp_f32_e32 v121, v121
	s_waitcnt lgkmcnt(2)
	v_mfma_scale_f32_32x32x64_f8f6f4 v[50:65], v[172:179], v[138:145], v[50:65], v247, v253 op_sel_hi:[0,0,0]
	v_exp_f32_e32 v122, v122
	v_exp_f32_e32 v123, v123
	v_exp_f32_e32 v124, v124
	v_exp_f32_e32 v125, v125
	v_exp_f32_e32 v126, v126
	v_exp_f32_e32 v127, v127
	v_exp_f32_e32 v128, v128
	v_exp_f32_e32 v129, v129
	s_waitcnt lgkmcnt(0)
	v_mfma_scale_f32_32x32x64_f8f6f4 v[82:97], v[164:171], v[138:145], v[82:97], v247, v253 op_sel_hi:[0,0,0]
	ds_read_b128 v[164:167], v157 offset:40960
	ds_read_b128 v[168:171], v157 offset:41984
	ds_read_b128 v[172:175], v157 offset:43008
	ds_read_b128 v[176:179], v157 offset:44032
	v_cvt_pk_bf8_f32 v180, v98, v99
	v_cvt_pk_bf8_f32 v181, v102, v103
	v_cvt_pk_bf8_f32 v182, v106, v107
	v_cvt_pk_bf8_f32 v183, v110, v111
	v_cvt_pk_bf8_f32 v184, v114, v115
	v_cvt_pk_bf8_f32 v185, v118, v119
	v_cvt_pk_bf8_f32 v186, v122, v123
	v_cvt_pk_bf8_f32 v187, v126, v127
	v_cvt_pk_bf8_f32 v180, v100, v101 op_sel:[0,0,1]
	v_cvt_pk_bf8_f32 v181, v104, v105 op_sel:[0,0,1]
	v_cvt_pk_bf8_f32 v182, v108, v109 op_sel:[0,0,1]
	v_cvt_pk_bf8_f32 v183, v112, v113 op_sel:[0,0,1]
	v_cvt_pk_bf8_f32 v184, v116, v117 op_sel:[0,0,1]
	v_cvt_pk_bf8_f32 v185, v120, v121 op_sel:[0,0,1]
	v_cvt_pk_bf8_f32 v186, v124, v125 op_sel:[0,0,1]
	v_cvt_pk_bf8_f32 v187, v128, v129 op_sel:[0,0,1]
	s_waitcnt lgkmcnt(2)
	v_mfma_scale_f32_32x32x64_f8f6f4 v[2:17], v[180:187], v[164:171], v[2:17], v251, v247 op_sel_hi:[0,0,0] cbsz:1
	s_waitcnt lgkmcnt(0)
	v_mfma_scale_f32_32x32x64_f8f6f4 v[34:49], v[180:187], v[196:203], v[34:49], v251, v251 op_sel_hi:[0,0,0] cbsz:1
